# s6 stack + attention causal-mask blocks via per-lane threshold, v_cmpx on shrinking EXEC + v_mov (2 VALU per element, no nops)
# speedup vs baseline: 1.0119x; 1.0013x over previous
; __device__ __forceinline__ void cmask(f32x16& p0, f32x16& p1, int jb, int qrel, int hi) {
;     const float NEG = -INFINITY; int kb = 64 * jb + 4 * hi;
; #pragma unroll
;     for (int r = 0; r < 16; ++r) { int kv = kb + (r & 3) + 8 * (r >> 2); if (kv > qrel) p0[r] = NEG; if (kv + 32 > qrel) p1[r] = NEG; }
; }
.LBB0_477:
	v_add_u32_e32 v184, s0, v230
	ds_read_b64_tr_b16 v[180:181], v184 offset:24576
	ds_read_b64_tr_b16 v[182:183], v184 offset:25088
	s_waitcnt lgkmcnt(9)
	v_mfma_f32_32x32x16_f16 v[48:63], v[176:179], v[128:131], v[48:63]
	v_add_f32_e32 v132, v80, v81
	v_add_f32_e32 v132, v82, v132
	v_add_f32_e32 v132, v83, v132
	v_add_f32_e32 v132, v84, v132
	v_add_f32_e32 v132, v85, v132
	v_cvt_pk_f16_f32 v144, v80, v81
	v_cvt_pk_f16_f32 v145, v82, v83
	ds_read_b64_tr_b16 v[176:177], v184 offset:28672
	ds_read_b64_tr_b16 v[178:179], v184 offset:29184
	s_waitcnt lgkmcnt(10)
	v_mfma_f32_32x32x16_f16 v[32:47], v[172:175], v[128:131], v[32:47]
	v_add_f32_e32 v80, v86, v132
	v_add_f32_e32 v80, v87, v80
	v_add_f32_e32 v80, v88, v80
	v_add_f32_e32 v80, v89, v80
	v_cvt_pk_f16_f32 v146, v84, v85
	v_cvt_pk_f16_f32 v147, v86, v87
	ds_read_b64_tr_b16 v[172:173], v184 offset:25600
	ds_read_b64_tr_b16 v[174:175], v184 offset:26112
	s_waitcnt lgkmcnt(11)
	v_mfma_f32_32x32x16_f16 v[48:63], v[168:171], v[124:127], v[48:63]
	v_add_f32_e32 v80, v90, v80
	v_add_f32_e32 v80, v91, v80
	v_add_f32_e32 v80, v92, v80
	v_add_f32_e32 v80, v93, v80
	v_cvt_pk_f16_f32 v140, v88, v89
	v_cvt_pk_f16_f32 v141, v90, v91
	ds_read_b64_tr_b16 v[84:85], v184 offset:29696
	ds_read_b64_tr_b16 v[86:87], v184 offset:30208
	s_waitcnt lgkmcnt(12)
	v_mfma_f32_32x32x16_f16 v[32:47], v[164:167], v[124:127], v[32:47]
	v_add_f32_e32 v80, v94, v80
	v_add_f32_e32 v80, v95, v80
	v_add_f32_e32 v80, v64, v80
	v_add_f32_e32 v88, v65, v80
	v_cvt_pk_f16_f32 v142, v92, v93
	v_cvt_pk_f16_f32 v143, v94, v95
	ds_read_b64_tr_b16 v[80:81], v184 offset:26624
	ds_read_b64_tr_b16 v[82:83], v184 offset:27136
	s_waitcnt lgkmcnt(13)
	v_mfma_f32_32x32x16_f16 v[48:63], v[160:163], v[120:123], v[48:63]
	v_add_f32_e32 v88, v66, v88
	v_add_f32_e32 v88, v67, v88
	v_add_f32_e32 v88, v68, v88
	v_add_f32_e32 v88, v69, v88
	v_cvt_pk_f16_f32 v136, v64, v65
	v_cvt_pk_f16_f32 v137, v66, v67
	ds_read_b64_tr_b16 v[160:161], v184 offset:30720
	ds_read_b64_tr_b16 v[162:163], v184 offset:31232
	s_waitcnt lgkmcnt(14)
	v_mfma_f32_32x32x16_f16 v[32:47], v[152:155], v[120:123], v[32:47]
	v_add_f32_e32 v64, v70, v88
	v_add_f32_e32 v64, v71, v64
	v_add_f32_e32 v64, v72, v64
	v_add_f32_e32 v88, v73, v64
	v_cvt_pk_f16_f32 v138, v68, v69
	v_cvt_pk_f16_f32 v139, v70, v71
	ds_read_b64_tr_b16 v[64:65], v184 offset:27648
	ds_read_b64_tr_b16 v[66:67], v184 offset:28160
	s_waitcnt lgkmcnt(14)
	v_mfma_f32_32x32x16_f16 v[48:63], v[156:159], v[116:119], v[48:63]
	v_add_f32_e32 v68, v74, v88
	v_add_f32_e32 v68, v75, v68
	v_add_f32_e32 v68, v76, v68
	v_add_f32_e32 v68, v77, v68
	v_cvt_pk_f16_f32 v132, v72, v73
	v_cvt_pk_f16_f32 v133, v74, v75
	ds_read_b64_tr_b16 v[152:153], v184 offset:31744
	ds_read_b64_tr_b16 v[154:155], v184 offset:32256
	v_mfma_f32_32x32x16_f16 v[32:47], v[148:151], v[116:119], v[32:47]
	v_add_f32_e32 v68, v78, v68
	v_add_f32_e32 v68, v79, v68
	v_add_f32_e32 v68, 0, v68
	v_cvt_pk_f16_f32 v134, v76, v77
	v_cvt_pk_f16_f32 v135, v78, v79
	s_add_i32 s0, s70, s89
	s_cmp_lt_u32 s69, 3
	s_cselect_b64 s[40:41], -1, 0
	s_mov_b32 s1, m0
	s_mov_b32 m0, s0
	s_nop 0
	global_load_lds_dwordx4 v[194:195], off
	s_mov_b32 m0, s1
	s_and_b64 s[0:1], s[40:41], exec
	s_cselect_b32 s18, s50, -3
	s_add_i32 s18, s18, s69
	v_mad_i64_i32 v[70:71], s[0:1], s18, v249, v[216:217]
	s_add_i32 s0, s68, s36
	s_mov_b32 s1, m0
	s_mov_b32 m0, s0
	s_nop 0
	global_load_lds_dwordx4 v[70:71], off
	s_mov_b32 m0, s1
	s_cmp_gt_u32 s69, 3
	s_cbranch_scc1 .LBB0_479
	s_mov_b64 s[100:101], exec
	v_sub_u32_e32 v70, v215, v197
	v_add_u32_e32 v70, 0x7b, v70
	v_cmpx_gt_i32_e32 59, v70
	v_mov_b32_e32 v47, v248
	v_cmpx_gt_i32_e32 58, v70
	v_mov_b32_e32 v46, v248
	v_cmpx_gt_i32_e32 57, v70
	v_mov_b32_e32 v45, v248
	v_cmpx_gt_i32_e32 56, v70
	v_mov_b32_e32 v44, v248
	v_cmpx_gt_i32_e32 51, v70
	v_mov_b32_e32 v43, v248
	v_cmpx_gt_i32_e32 50, v70
	v_mov_b32_e32 v42, v248
	v_cmpx_gt_i32_e32 49, v70
	v_mov_b32_e32 v41, v248
	v_cmpx_gt_i32_e32 48, v70
	v_mov_b32_e32 v40, v248
	v_cmpx_gt_i32_e32 43, v70
	v_mov_b32_e32 v39, v248
	v_cmpx_gt_i32_e32 42, v70
	v_mov_b32_e32 v38, v248
	v_cmpx_gt_i32_e32 41, v70
	v_mov_b32_e32 v37, v248
	v_cmpx_gt_i32_e32 40, v70
	v_mov_b32_e32 v36, v248
	v_cmpx_gt_i32_e32 35, v70
	v_mov_b32_e32 v35, v248
	v_cmpx_gt_i32_e32 34, v70
	v_mov_b32_e32 v34, v248
	v_cmpx_gt_i32_e32 33, v70
	v_mov_b32_e32 v33, v248
	v_cmpx_gt_i32_e32 32, v70
	v_mov_b32_e32 v32, v248
	v_cmpx_gt_i32_e32 27, v70
	v_mov_b32_e32 v63, v248
	v_cmpx_gt_i32_e32 26, v70
	v_mov_b32_e32 v62, v248
	v_cmpx_gt_i32_e32 25, v70
	v_mov_b32_e32 v61, v248
	v_cmpx_gt_i32_e32 24, v70
	v_mov_b32_e32 v60, v248
	v_cmpx_gt_i32_e32 19, v70
	v_mov_b32_e32 v59, v248
	v_cmpx_gt_i32_e32 18, v70
	v_mov_b32_e32 v58, v248
	v_cmpx_gt_i32_e32 17, v70
	v_mov_b32_e32 v57, v248
	v_cmpx_gt_i32_e32 16, v70
	v_mov_b32_e32 v56, v248
	v_cmpx_gt_i32_e32 11, v70
	v_mov_b32_e32 v55, v248
	v_cmpx_gt_i32_e32 10, v70
	v_mov_b32_e32 v54, v248
	v_cmpx_gt_i32_e32 9, v70
	v_mov_b32_e32 v53, v248
	v_cmpx_gt_i32_e32 8, v70
	v_mov_b32_e32 v52, v248
	v_cmpx_gt_i32_e32 3, v70
	v_mov_b32_e32 v51, v248
	v_cmpx_gt_i32_e32 2, v70
	v_mov_b32_e32 v50, v248
	v_cmpx_gt_i32_e32 1, v70
	v_mov_b32_e32 v49, v248
	v_cmpx_gt_i32_e32 0, v70
	v_mov_b32_e32 v48, v248
	s_mov_b64 exec, s[100:101]
	s_nop 4

; __device__ __forceinline__ void cmask(f32x16& p0, f32x16& p1, int jb, int qrel, int hi) {
;     const float NEG = -INFINITY; int kb = 64 * jb + 4 * hi;
; #pragma unroll
;     for (int r = 0; r < 16; ++r) { int kv = kb + (r & 3) + 8 * (r >> 2); if (kv > qrel) p0[r] = NEG; if (kv + 32 > qrel) p1[r] = NEG; }
; }
.LBB0_482:
	s_add_i32 s0, s68, 0x2000
	s_cmpk_lg_i32 s68, 0x4000
	s_cselect_b32 s45, s0, 0
	v_add_u32_e32 v160, s70, v230
	ds_read_b64_tr_b16 v[156:157], v160 offset:24576
	ds_read_b64_tr_b16 v[158:159], v160 offset:25088
	v_mfma_f32_32x32x16_f16 v[80:95], v[188:191], v[128:131], v[80:95]
	v_add_f32_e32 v132, v48, v49
	v_add_f32_e32 v132, v50, v132
	v_add_f32_e32 v132, v51, v132
	v_add_f32_e32 v132, v52, v132
	v_add_f32_e32 v132, v53, v132
	v_cvt_pk_f16_f32 v144, v48, v49
	v_cvt_pk_f16_f32 v145, v50, v51
	ds_read_b64_tr_b16 v[152:153], v160 offset:28672
	ds_read_b64_tr_b16 v[154:155], v160 offset:29184
	v_mfma_f32_32x32x16_f16 v[64:79], v[148:151], v[128:131], v[64:79]
	v_add_f32_e32 v48, v54, v132
	v_add_f32_e32 v48, v55, v48
	v_add_f32_e32 v48, v56, v48
	v_add_f32_e32 v48, v57, v48
	v_cvt_pk_f16_f32 v146, v52, v53
	v_cvt_pk_f16_f32 v147, v54, v55
	ds_read_b64_tr_b16 v[148:149], v160 offset:25600
	ds_read_b64_tr_b16 v[150:151], v160 offset:26112
	v_mfma_f32_32x32x16_f16 v[80:95], v[184:187], v[124:127], v[80:95]
	v_add_f32_e32 v48, v58, v48
	v_add_f32_e32 v48, v59, v48
	v_add_f32_e32 v48, v60, v48
	v_add_f32_e32 v48, v61, v48
	v_cvt_pk_f16_f32 v140, v56, v57
	v_cvt_pk_f16_f32 v141, v58, v59
	ds_read_b64_tr_b16 v[52:53], v160 offset:29696
	ds_read_b64_tr_b16 v[54:55], v160 offset:30208
	v_mfma_f32_32x32x16_f16 v[64:79], v[172:175], v[124:127], v[64:79]
	v_add_f32_e32 v48, v62, v48
	v_add_f32_e32 v48, v63, v48
	v_add_f32_e32 v48, v32, v48
	v_add_f32_e32 v56, v33, v48
	v_cvt_pk_f16_f32 v142, v60, v61
	v_cvt_pk_f16_f32 v143, v62, v63
	ds_read_b64_tr_b16 v[48:49], v160 offset:26624
	ds_read_b64_tr_b16 v[50:51], v160 offset:27136
	s_waitcnt lgkmcnt(13)
	v_mfma_f32_32x32x16_f16 v[80:95], v[176:179], v[120:123], v[80:95]
	v_add_f32_e32 v56, v34, v56
	v_add_f32_e32 v56, v35, v56
	v_add_f32_e32 v56, v36, v56
	v_add_f32_e32 v56, v37, v56
	v_cvt_pk_f16_f32 v136, v32, v33
	v_cvt_pk_f16_f32 v137, v34, v35
	ds_read_b64_tr_b16 v[184:185], v160 offset:30720
	ds_read_b64_tr_b16 v[186:187], v160 offset:31232
	s_waitcnt lgkmcnt(14)
	v_mfma_f32_32x32x16_f16 v[64:79], v[164:167], v[120:123], v[64:79]
	v_add_f32_e32 v32, v38, v56
	v_add_f32_e32 v32, v39, v32
	v_add_f32_e32 v32, v40, v32
	v_add_f32_e32 v56, v41, v32
	v_cvt_pk_f16_f32 v138, v36, v37
	v_cvt_pk_f16_f32 v139, v38, v39
	ds_read_b64_tr_b16 v[32:33], v160 offset:27648
	ds_read_b64_tr_b16 v[34:35], v160 offset:28160
	s_waitcnt lgkmcnt(14)
	v_mfma_f32_32x32x16_f16 v[80:95], v[180:183], v[116:119], v[80:95]
	v_add_f32_e32 v36, v42, v56
	v_add_f32_e32 v36, v43, v36
	v_add_f32_e32 v36, v44, v36
	v_add_f32_e32 v36, v45, v36
	v_cvt_pk_f16_f32 v132, v40, v41
	v_cvt_pk_f16_f32 v133, v42, v43
	ds_read_b64_tr_b16 v[180:181], v160 offset:31744
	ds_read_b64_tr_b16 v[182:183], v160 offset:32256
	v_mfma_f32_32x32x16_f16 v[64:79], v[168:171], v[116:119], v[64:79]
	v_add_f32_e32 v36, v46, v36
	v_add_f32_e32 v36, v47, v36
	v_add_f32_e32 v36, 0, v36
	v_cvt_pk_f16_f32 v134, v44, v45
	v_cvt_pk_f16_f32 v135, v46, v47
	s_add_i32 s0, s68, s89
	v_lshl_add_u64 v[38:39], v[194:195], 0, s[30:31]
	s_mov_b32 s1, m0
	s_mov_b32 m0, s0
	s_nop 0
	global_load_lds_dwordx4 v[38:39], off
	s_mov_b32 m0, s1
	s_cmp_lt_u32 s69, 2
	s_cselect_b64 s[0:1], -1, 0
	s_and_b64 s[18:19], s[0:1], exec
	s_cselect_b32 s18, s51, -2
	s_add_i32 s18, s18, s69
	v_mad_i64_i32 v[38:39], s[46:47], s18, v249, v[216:217]
	s_add_i32 s19, s45, s36
	s_mov_b32 s46, m0
	s_mov_b32 m0, s19
	s_nop 0
	global_load_lds_dwordx4 v[38:39], off
	s_mov_b32 m0, s46
	s_andn2_b64 vcc, exec, s[40:41]
	s_cbranch_vccnz .LBB0_484
	s_mov_b64 s[100:101], exec
	v_sub_u32_e32 v38, v215, v197
	v_add_u32_e32 v38, 59, v38
	v_cmpx_gt_i32_e32 59, v38
	v_mov_b32_e32 v79, v248
	v_cmpx_gt_i32_e32 58, v38
	v_mov_b32_e32 v78, v248
	v_cmpx_gt_i32_e32 57, v38
	v_mov_b32_e32 v77, v248
	v_cmpx_gt_i32_e32 56, v38
	v_mov_b32_e32 v76, v248
	v_cmpx_gt_i32_e32 51, v38
	v_mov_b32_e32 v75, v248
	v_cmpx_gt_i32_e32 50, v38
	v_mov_b32_e32 v74, v248
	v_cmpx_gt_i32_e32 49, v38
	v_mov_b32_e32 v73, v248
	v_cmpx_gt_i32_e32 48, v38
	v_mov_b32_e32 v72, v248
	v_cmpx_gt_i32_e32 43, v38
	v_mov_b32_e32 v71, v248
	v_cmpx_gt_i32_e32 42, v38
	v_mov_b32_e32 v70, v248
	v_cmpx_gt_i32_e32 41, v38
	v_mov_b32_e32 v69, v248
	v_cmpx_gt_i32_e32 40, v38
	v_mov_b32_e32 v68, v248
	v_cmpx_gt_i32_e32 35, v38
	v_mov_b32_e32 v67, v248
	v_cmpx_gt_i32_e32 34, v38
	v_mov_b32_e32 v66, v248
	v_cmpx_gt_i32_e32 33, v38
	v_mov_b32_e32 v65, v248
	v_cmpx_gt_i32_e32 32, v38
	v_mov_b32_e32 v64, v248
	v_cmpx_gt_i32_e32 27, v38
	v_mov_b32_e32 v95, v248
	v_cmpx_gt_i32_e32 26, v38
	v_mov_b32_e32 v94, v248
	v_cmpx_gt_i32_e32 25, v38
	v_mov_b32_e32 v93, v248
	v_cmpx_gt_i32_e32 24, v38
	v_mov_b32_e32 v92, v248
	v_cmpx_gt_i32_e32 19, v38
	v_mov_b32_e32 v91, v248
	v_cmpx_gt_i32_e32 18, v38
	v_mov_b32_e32 v90, v248
	v_cmpx_gt_i32_e32 17, v38
	v_mov_b32_e32 v89, v248
	v_cmpx_gt_i32_e32 16, v38
	v_mov_b32_e32 v88, v248
	v_cmpx_gt_i32_e32 11, v38
	v_mov_b32_e32 v87, v248
	v_cmpx_gt_i32_e32 10, v38
	v_mov_b32_e32 v86, v248
	v_cmpx_gt_i32_e32 9, v38
	v_mov_b32_e32 v85, v248
	v_cmpx_gt_i32_e32 8, v38
	v_mov_b32_e32 v84, v248
	v_cmpx_gt_i32_e32 3, v38
	v_mov_b32_e32 v83, v248
	v_cmpx_gt_i32_e32 2, v38
	v_mov_b32_e32 v82, v248
	v_cmpx_gt_i32_e32 1, v38
	v_mov_b32_e32 v81, v248
	v_cmpx_gt_i32_e32 0, v38
	v_mov_b32_e32 v80, v248
	s_mov_b64 exec, s[100:101]
	s_nop 4

; __device__ __forceinline__ void cmask(f32x16& p0, f32x16& p1, int jb, int qrel, int hi) {
;     const float NEG = -INFINITY; int kb = 64 * jb + 4 * hi;
; #pragma unroll
;     for (int r = 0; r < 16; ++r) { int kv = kb + (r & 3) + 8 * (r >> 2); if (kv > qrel) p0[r] = NEG; if (kv + 32 > qrel) p1[r] = NEG; }
; }
.LBB0_500:
	s_add_i32 s68, s26, s19
	s_add_i32 s0, s68, 1
	v_mov_b32_e32 v68, s0
	v_sub_co_u32_e64 v70, s[40:41], s19, 3
	s_nop 1
	v_cndmask_b32_e64 v68, v70, v68, s[40:41]
	v_mad_i64_i32 v[70:71], s[0:1], v68, s48, v[216:217]
	s_add_i32 s0, s18, s36
	s_mov_b32 s1, m0
	s_mov_b32 m0, s0
	s_nop 0
	global_load_lds_dwordx4 v[70:71], off
	s_mov_b32 m0, s1
	s_cmp_gt_u32 s19, 3
	s_cbranch_scc1 .LBB0_502
	s_mov_b64 s[100:101], exec
	v_sub_u32_e32 v71, v215, v237
	v_add_u32_e32 v71, 0x7b, v71
	v_cmpx_gt_i32_e32 59, v71
	v_mov_b32_e32 v47, v248
	v_cmpx_gt_i32_e32 58, v71
	v_mov_b32_e32 v46, v248
	v_cmpx_gt_i32_e32 57, v71
	v_mov_b32_e32 v45, v248
	v_cmpx_gt_i32_e32 56, v71
	v_mov_b32_e32 v44, v248
	v_cmpx_gt_i32_e32 51, v71
	v_mov_b32_e32 v43, v248
	v_cmpx_gt_i32_e32 50, v71
	v_mov_b32_e32 v42, v248
	v_cmpx_gt_i32_e32 49, v71
	v_mov_b32_e32 v41, v248
	v_cmpx_gt_i32_e32 48, v71
	v_mov_b32_e32 v40, v248
	v_cmpx_gt_i32_e32 43, v71
	v_mov_b32_e32 v39, v248
	v_cmpx_gt_i32_e32 42, v71
	v_mov_b32_e32 v38, v248
	v_cmpx_gt_i32_e32 41, v71
	v_mov_b32_e32 v37, v248
	v_cmpx_gt_i32_e32 40, v71
	v_mov_b32_e32 v36, v248
	v_cmpx_gt_i32_e32 35, v71
	v_mov_b32_e32 v35, v248
	v_cmpx_gt_i32_e32 34, v71
	v_mov_b32_e32 v34, v248
	v_cmpx_gt_i32_e32 33, v71
	v_mov_b32_e32 v33, v248
	v_cmpx_gt_i32_e32 32, v71
	v_mov_b32_e32 v32, v248
	v_cmpx_gt_i32_e32 27, v71
	v_mov_b32_e32 v63, v248
	v_cmpx_gt_i32_e32 26, v71
	v_mov_b32_e32 v62, v248
	v_cmpx_gt_i32_e32 25, v71
	v_mov_b32_e32 v61, v248
	v_cmpx_gt_i32_e32 24, v71
	v_mov_b32_e32 v60, v248
	v_cmpx_gt_i32_e32 19, v71
	v_mov_b32_e32 v59, v248
	v_cmpx_gt_i32_e32 18, v71
	v_mov_b32_e32 v58, v248
	v_cmpx_gt_i32_e32 17, v71
	v_mov_b32_e32 v57, v248
	v_cmpx_gt_i32_e32 16, v71
	v_mov_b32_e32 v56, v248
	v_cmpx_gt_i32_e32 11, v71
	v_mov_b32_e32 v55, v248
	v_cmpx_gt_i32_e32 10, v71
	v_mov_b32_e32 v54, v248
	v_cmpx_gt_i32_e32 9, v71
	v_mov_b32_e32 v53, v248
	v_cmpx_gt_i32_e32 8, v71
	v_mov_b32_e32 v52, v248
	v_cmpx_gt_i32_e32 3, v71
	v_mov_b32_e32 v51, v248
	v_cmpx_gt_i32_e32 2, v71
	v_mov_b32_e32 v50, v248
	v_cmpx_gt_i32_e32 1, v71
	v_mov_b32_e32 v49, v248
	v_cmpx_gt_i32_e32 0, v71
	v_mov_b32_e32 v48, v248
	s_mov_b64 exec, s[100:101]
	s_nop 4

; __device__ __forceinline__ void cmask(f32x16& p0, f32x16& p1, int jb, int qrel, int hi) {
;     const float NEG = -INFINITY; int kb = 64 * jb + 4 * hi;
; #pragma unroll
;     for (int r = 0; r < 16; ++r) { int kv = kb + (r & 3) + 8 * (r >> 2); if (kv > qrel) p0[r] = NEG; if (kv + 32 > qrel) p1[r] = NEG; }
; }
.LBB0_511:
	s_andn2_b64 vcc, exec, s[40:41]
	s_cbranch_vccnz .LBB0_513
	s_mov_b64 s[100:101], exec
	v_sub_u32_e32 v240, v215, v237
	v_add_u32_e32 v240, 59, v240
	v_cmpx_gt_i32_e32 59, v240
	v_mov_b32_e32 v79, v248
	v_cmpx_gt_i32_e32 58, v240
	v_mov_b32_e32 v78, v248
	v_cmpx_gt_i32_e32 57, v240
	v_mov_b32_e32 v77, v248
	v_cmpx_gt_i32_e32 56, v240
	v_mov_b32_e32 v76, v248
	v_cmpx_gt_i32_e32 51, v240
	v_mov_b32_e32 v75, v248
	v_cmpx_gt_i32_e32 50, v240
	v_mov_b32_e32 v74, v248
	v_cmpx_gt_i32_e32 49, v240
	v_mov_b32_e32 v73, v248
	v_cmpx_gt_i32_e32 48, v240
	v_mov_b32_e32 v72, v248
	v_cmpx_gt_i32_e32 43, v240
	v_mov_b32_e32 v71, v248
	v_cmpx_gt_i32_e32 42, v240
	v_mov_b32_e32 v70, v248
	v_cmpx_gt_i32_e32 41, v240
	v_mov_b32_e32 v69, v248
	v_cmpx_gt_i32_e32 40, v240
	v_mov_b32_e32 v68, v248
	v_cmpx_gt_i32_e32 35, v240
	v_mov_b32_e32 v67, v248
	v_cmpx_gt_i32_e32 34, v240
	v_mov_b32_e32 v66, v248
	v_cmpx_gt_i32_e32 33, v240
	v_mov_b32_e32 v65, v248
	v_cmpx_gt_i32_e32 32, v240
	v_mov_b32_e32 v64, v248
	v_cmpx_gt_i32_e32 27, v240
	v_mov_b32_e32 v95, v248
	v_cmpx_gt_i32_e32 26, v240
	v_mov_b32_e32 v94, v248
	v_cmpx_gt_i32_e32 25, v240
	v_mov_b32_e32 v93, v248
	v_cmpx_gt_i32_e32 24, v240
	v_mov_b32_e32 v92, v248
	v_cmpx_gt_i32_e32 19, v240
	v_mov_b32_e32 v91, v248
	v_cmpx_gt_i32_e32 18, v240
	v_mov_b32_e32 v90, v248
	v_cmpx_gt_i32_e32 17, v240
	v_mov_b32_e32 v89, v248
	v_cmpx_gt_i32_e32 16, v240
	v_mov_b32_e32 v88, v248
	v_cmpx_gt_i32_e32 11, v240
	v_mov_b32_e32 v87, v248
	v_cmpx_gt_i32_e32 10, v240
	v_mov_b32_e32 v86, v248
	v_cmpx_gt_i32_e32 9, v240
	v_mov_b32_e32 v85, v248
	v_cmpx_gt_i32_e32 8, v240
	v_mov_b32_e32 v84, v248
	v_cmpx_gt_i32_e32 3, v240
	v_mov_b32_e32 v83, v248
	v_cmpx_gt_i32_e32 2, v240
	v_mov_b32_e32 v82, v248
	v_cmpx_gt_i32_e32 1, v240
	v_mov_b32_e32 v81, v248
	v_cmpx_gt_i32_e32 0, v240
	v_mov_b32_e32 v80, v248
	s_mov_b64 exec, s[100:101]
	s_nop 4

; __device__ __forceinline__ void cmask(f32x16& p0, f32x16& p1, int jb, int qrel, int hi) {
;     const float NEG = -INFINITY; int kb = 64 * jb + 4 * hi;
; #pragma unroll
;     for (int r = 0; r < 16; ++r) { int kv = kb + (r & 3) + 8 * (r >> 2); if (kv > qrel) p0[r] = NEG; if (kv + 32 > qrel) p1[r] = NEG; }
; }
.LBB0_565:
	v_add_u32_e32 v184, s18, v230
	ds_read_b64_tr_b16 v[180:181], v184 offset:24576
	ds_read_b64_tr_b16 v[182:183], v184 offset:25088
	s_waitcnt lgkmcnt(9)
	v_mfma_f32_32x32x16_f16 v[48:63], v[176:179], v[128:131], v[48:63]
	v_add_f32_e32 v132, v80, v81
	v_add_f32_e32 v132, v82, v132
	v_add_f32_e32 v132, v83, v132
	v_add_f32_e32 v132, v84, v132
	v_add_f32_e32 v132, v85, v132
	v_cvt_pk_f16_f32 v144, v80, v81
	v_cvt_pk_f16_f32 v145, v82, v83
	ds_read_b64_tr_b16 v[80:81], v184 offset:28672
	ds_read_b64_tr_b16 v[82:83], v184 offset:29184
	s_waitcnt lgkmcnt(10)
	v_mfma_f32_32x32x16_f16 v[32:47], v[172:175], v[128:131], v[32:47]
	v_add_f32_e32 v128, v86, v132
	v_add_f32_e32 v128, v87, v128
	v_add_f32_e32 v128, v88, v128
	v_add_f32_e32 v128, v89, v128
	v_cvt_pk_f16_f32 v146, v84, v85
	v_cvt_pk_f16_f32 v147, v86, v87
	ds_read_b64_tr_b16 v[84:85], v184 offset:25600
	ds_read_b64_tr_b16 v[86:87], v184 offset:26112
	s_waitcnt lgkmcnt(11)
	v_mfma_f32_32x32x16_f16 v[48:63], v[168:171], v[124:127], v[48:63]
	v_add_f32_e32 v128, v90, v128
	v_add_f32_e32 v128, v91, v128
	v_add_f32_e32 v128, v92, v128
	v_add_f32_e32 v128, v93, v128
	v_cvt_pk_f16_f32 v140, v88, v89
	v_cvt_pk_f16_f32 v141, v90, v91
	ds_read_b64_tr_b16 v[88:89], v184 offset:29696
	ds_read_b64_tr_b16 v[90:91], v184 offset:30208
	s_waitcnt lgkmcnt(12)
	v_mfma_f32_32x32x16_f16 v[32:47], v[164:167], v[124:127], v[32:47]
	v_add_f32_e32 v124, v94, v128
	v_add_f32_e32 v124, v95, v124
	v_add_f32_e32 v124, v64, v124
	v_add_f32_e32 v124, v65, v124
	v_cvt_pk_f16_f32 v142, v92, v93
	v_cvt_pk_f16_f32 v143, v94, v95
	ds_read_b64_tr_b16 v[92:93], v184 offset:26624
	ds_read_b64_tr_b16 v[94:95], v184 offset:27136
	s_waitcnt lgkmcnt(13)
	v_mfma_f32_32x32x16_f16 v[48:63], v[160:163], v[120:123], v[48:63]
	v_add_f32_e32 v124, v66, v124
	v_add_f32_e32 v124, v67, v124
	v_add_f32_e32 v124, v68, v124
	v_add_f32_e32 v124, v69, v124
	v_cvt_pk_f16_f32 v136, v64, v65
	v_cvt_pk_f16_f32 v137, v66, v67
	ds_read_b64_tr_b16 v[64:65], v184 offset:30720
	ds_read_b64_tr_b16 v[66:67], v184 offset:31232
	s_waitcnt lgkmcnt(14)
	v_mfma_f32_32x32x16_f16 v[32:47], v[152:155], v[120:123], v[32:47]
	v_add_f32_e32 v120, v70, v124
	v_add_f32_e32 v120, v71, v120
	v_add_f32_e32 v120, v72, v120
	v_add_f32_e32 v120, v73, v120
	v_cvt_pk_f16_f32 v138, v68, v69
	v_cvt_pk_f16_f32 v139, v70, v71
	ds_read_b64_tr_b16 v[68:69], v184 offset:27648
	ds_read_b64_tr_b16 v[70:71], v184 offset:28160
	s_waitcnt lgkmcnt(14)
	v_mfma_f32_32x32x16_f16 v[48:63], v[156:159], v[116:119], v[48:63]
	v_add_f32_e32 v120, v74, v120
	v_add_f32_e32 v120, v75, v120
	v_add_f32_e32 v120, v76, v120
	v_add_f32_e32 v120, v77, v120
	v_cvt_pk_f16_f32 v132, v72, v73
	v_cvt_pk_f16_f32 v133, v74, v75
	ds_read_b64_tr_b16 v[72:73], v184 offset:31744
	ds_read_b64_tr_b16 v[74:75], v184 offset:32256
	v_mfma_f32_32x32x16_f16 v[32:47], v[148:151], v[116:119], v[32:47]
	v_add_f32_e32 v116, v78, v120
	v_add_f32_e32 v116, v79, v116
	v_add_f32_e32 v116, 0, v116
	v_cvt_pk_f16_f32 v134, v76, v77
	v_cvt_pk_f16_f32 v135, v78, v79
	s_andn2_b64 vcc, exec, s[42:43]
	s_cbranch_vccnz .LBB0_567
	s_mov_b64 s[100:101], exec
	v_sub_u32_e32 v77, v215, v233
	v_add_u32_e32 v77, 0xffffff40, v77
	v_cmpx_gt_i32_e32 59, v77
	v_mov_b32_e32 v47, v248
	v_cmpx_gt_i32_e32 58, v77
	v_mov_b32_e32 v46, v248
	v_cmpx_gt_i32_e32 57, v77
	v_mov_b32_e32 v45, v248
	v_cmpx_gt_i32_e32 56, v77
	v_mov_b32_e32 v44, v248
	v_cmpx_gt_i32_e32 51, v77
	v_mov_b32_e32 v43, v248
	v_cmpx_gt_i32_e32 50, v77
	v_mov_b32_e32 v42, v248
	v_cmpx_gt_i32_e32 49, v77
	v_mov_b32_e32 v41, v248
	v_cmpx_gt_i32_e32 48, v77
	v_mov_b32_e32 v40, v248
	v_cmpx_gt_i32_e32 43, v77
	v_mov_b32_e32 v39, v248
	v_cmpx_gt_i32_e32 42, v77
	v_mov_b32_e32 v38, v248
	v_cmpx_gt_i32_e32 41, v77
	v_mov_b32_e32 v37, v248
	v_cmpx_gt_i32_e32 40, v77
	v_mov_b32_e32 v36, v248
	v_cmpx_gt_i32_e32 35, v77
	v_mov_b32_e32 v35, v248
	v_cmpx_gt_i32_e32 34, v77
	v_mov_b32_e32 v34, v248
	v_cmpx_gt_i32_e32 33, v77
	v_mov_b32_e32 v33, v248
	v_cmpx_gt_i32_e32 32, v77
	v_mov_b32_e32 v32, v248
	v_cmpx_gt_i32_e32 27, v77
	v_mov_b32_e32 v63, v248
	v_cmpx_gt_i32_e32 26, v77
	v_mov_b32_e32 v62, v248
	v_cmpx_gt_i32_e32 25, v77
	v_mov_b32_e32 v61, v248
	v_cmpx_gt_i32_e32 24, v77
	v_mov_b32_e32 v60, v248
	v_cmpx_gt_i32_e32 19, v77
	v_mov_b32_e32 v59, v248
	v_cmpx_gt_i32_e32 18, v77
	v_mov_b32_e32 v58, v248
	v_cmpx_gt_i32_e32 17, v77
	v_mov_b32_e32 v57, v248
	v_cmpx_gt_i32_e32 16, v77
	v_mov_b32_e32 v56, v248
	v_cmpx_gt_i32_e32 11, v77
	v_mov_b32_e32 v55, v248
	v_cmpx_gt_i32_e32 10, v77
	v_mov_b32_e32 v54, v248
	v_cmpx_gt_i32_e32 9, v77
	v_mov_b32_e32 v53, v248
	v_cmpx_gt_i32_e32 8, v77
	v_mov_b32_e32 v52, v248
	v_cmpx_gt_i32_e32 3, v77
	v_mov_b32_e32 v51, v248
	v_cmpx_gt_i32_e32 2, v77
	v_mov_b32_e32 v50, v248
	v_cmpx_gt_i32_e32 1, v77
	v_mov_b32_e32 v49, v248
	v_cmpx_gt_i32_e32 0, v77
	v_mov_b32_e32 v48, v248
	s_mov_b64 exec, s[100:101]
	s_nop 4

; __device__ __forceinline__ void cmask(f32x16& p0, f32x16& p1, int jb, int qrel, int hi) {
;     const float NEG = -INFINITY; int kb = 64 * jb + 4 * hi;
; #pragma unroll
;     for (int r = 0; r < 16; ++r) { int kv = kb + (r & 3) + 8 * (r >> 2); if (kv > qrel) p0[r] = NEG; if (kv + 32 > qrel) p1[r] = NEG; }
; }
.LBB0_625:
	v_add_u32_e32 v184, s40, v229
	ds_read_b64_tr_b16 v[180:181], v184 offset:24576
	ds_read_b64_tr_b16 v[182:183], v184 offset:25088
	s_waitcnt lgkmcnt(9)
	v_mfma_f32_32x32x16_f16 v[48:63], v[176:179], v[128:131], v[48:63]
	v_add_f32_e32 v132, v80, v81
	v_add_f32_e32 v132, v82, v132
	v_add_f32_e32 v132, v83, v132
	v_add_f32_e32 v132, v84, v132
	v_add_f32_e32 v132, v85, v132
	v_cvt_pk_f16_f32 v144, v80, v81
	v_cvt_pk_f16_f32 v145, v82, v83
	ds_read_b64_tr_b16 v[176:177], v184 offset:28672
	ds_read_b64_tr_b16 v[178:179], v184 offset:29184
	s_waitcnt lgkmcnt(10)
	v_mfma_f32_32x32x16_f16 v[32:47], v[172:175], v[128:131], v[32:47]
	v_add_f32_e32 v80, v86, v132
	v_add_f32_e32 v80, v87, v80
	v_add_f32_e32 v80, v88, v80
	v_add_f32_e32 v80, v89, v80
	v_cvt_pk_f16_f32 v146, v84, v85
	v_cvt_pk_f16_f32 v147, v86, v87
	ds_read_b64_tr_b16 v[172:173], v184 offset:25600
	ds_read_b64_tr_b16 v[174:175], v184 offset:26112
	s_waitcnt lgkmcnt(11)
	v_mfma_f32_32x32x16_f16 v[48:63], v[168:171], v[124:127], v[48:63]
	v_add_f32_e32 v80, v90, v80
	v_add_f32_e32 v80, v91, v80
	v_add_f32_e32 v80, v92, v80
	v_add_f32_e32 v80, v93, v80
	v_cvt_pk_f16_f32 v140, v88, v89
	v_cvt_pk_f16_f32 v141, v90, v91
	ds_read_b64_tr_b16 v[84:85], v184 offset:29696
	ds_read_b64_tr_b16 v[86:87], v184 offset:30208
	s_waitcnt lgkmcnt(12)
	v_mfma_f32_32x32x16_f16 v[32:47], v[164:167], v[124:127], v[32:47]
	v_add_f32_e32 v80, v94, v80
	v_add_f32_e32 v80, v95, v80
	v_add_f32_e32 v80, v64, v80
	v_add_f32_e32 v88, v65, v80
	v_cvt_pk_f16_f32 v142, v92, v93
	v_cvt_pk_f16_f32 v143, v94, v95
	ds_read_b64_tr_b16 v[80:81], v184 offset:26624
	ds_read_b64_tr_b16 v[82:83], v184 offset:27136
	s_waitcnt lgkmcnt(13)
	v_mfma_f32_32x32x16_f16 v[48:63], v[160:163], v[120:123], v[48:63]
	v_add_f32_e32 v88, v66, v88
	v_add_f32_e32 v88, v67, v88
	v_add_f32_e32 v88, v68, v88
	v_add_f32_e32 v88, v69, v88
	v_cvt_pk_f16_f32 v136, v64, v65
	v_cvt_pk_f16_f32 v137, v66, v67
	ds_read_b64_tr_b16 v[160:161], v184 offset:30720
	ds_read_b64_tr_b16 v[162:163], v184 offset:31232
	s_waitcnt lgkmcnt(14)
	v_mfma_f32_32x32x16_f16 v[32:47], v[152:155], v[120:123], v[32:47]
	v_add_f32_e32 v64, v70, v88
	v_add_f32_e32 v64, v71, v64
	v_add_f32_e32 v64, v72, v64
	v_add_f32_e32 v88, v73, v64
	v_cvt_pk_f16_f32 v138, v68, v69
	v_cvt_pk_f16_f32 v139, v70, v71
	ds_read_b64_tr_b16 v[64:65], v184 offset:27648
	ds_read_b64_tr_b16 v[66:67], v184 offset:28160
	s_waitcnt lgkmcnt(14)
	v_mfma_f32_32x32x16_f16 v[48:63], v[156:159], v[116:119], v[48:63]
	v_add_f32_e32 v68, v74, v88
	v_add_f32_e32 v68, v75, v68
	v_add_f32_e32 v68, v76, v68
	v_add_f32_e32 v68, v77, v68
	v_cvt_pk_f16_f32 v132, v72, v73
	v_cvt_pk_f16_f32 v133, v74, v75
	ds_read_b64_tr_b16 v[152:153], v184 offset:31744
	ds_read_b64_tr_b16 v[154:155], v184 offset:32256
	v_mfma_f32_32x32x16_f16 v[32:47], v[148:151], v[116:119], v[32:47]
	v_add_f32_e32 v68, v78, v68
	v_add_f32_e32 v68, v79, v68
	v_add_f32_e32 v68, 0, v68
	v_cvt_pk_f16_f32 v134, v76, v77
	v_cvt_pk_f16_f32 v135, v78, v79
	v_lshl_add_u64 v[70:71], v[194:195], 0, s[30:31]
	s_add_i32 s11, s69, s90
	s_mov_b32 s18, m0
	s_mov_b32 m0, s11
	s_nop 0
	global_load_lds_dwordx4 v[70:71], off
	s_mov_b32 m0, s18
	s_add_i32 s18, s26, s45
	s_add_i32 s37, s26, s19
	s_add_i32 s11, s18, 1
	s_add_i32 s66, s37, 1
	s_cmp_lt_u32 s45, 3
	s_cselect_b64 s[40:41], -1, 0
	s_and_b64 s[50:51], s[40:41], exec
	s_cselect_b32 s11, s11, s66
	v_mad_i64_i32 v[70:71], s[50:51], s11, v249, v[216:217]
	s_add_i32 s50, s68, s10
	s_mov_b32 s51, m0
	s_mov_b32 m0, s50
	s_nop 0
	global_load_lds_dwordx4 v[70:71], off
	s_mov_b32 m0, s51
	s_cmp_gt_u32 s45, 3
	s_cbranch_scc1 .LBB0_627
	s_mov_b64 s[100:101], exec
	v_sub_u32_e32 v69, v215, v196
	v_add_u32_e32 v69, 32, v69
	v_cmpx_gt_i32_e32 59, v69
	v_mov_b32_e32 v47, v248
	v_cmpx_gt_i32_e32 58, v69
	v_mov_b32_e32 v46, v248
	v_cmpx_gt_i32_e32 57, v69
	v_mov_b32_e32 v45, v248
	v_cmpx_gt_i32_e32 56, v69
	v_mov_b32_e32 v44, v248
	v_cmpx_gt_i32_e32 51, v69
	v_mov_b32_e32 v43, v248
	v_cmpx_gt_i32_e32 50, v69
	v_mov_b32_e32 v42, v248
	v_cmpx_gt_i32_e32 49, v69
	v_mov_b32_e32 v41, v248
	v_cmpx_gt_i32_e32 48, v69
	v_mov_b32_e32 v40, v248
	v_cmpx_gt_i32_e32 43, v69
	v_mov_b32_e32 v39, v248
	v_cmpx_gt_i32_e32 42, v69
	v_mov_b32_e32 v38, v248
	v_cmpx_gt_i32_e32 41, v69
	v_mov_b32_e32 v37, v248
	v_cmpx_gt_i32_e32 40, v69
	v_mov_b32_e32 v36, v248
	v_cmpx_gt_i32_e32 35, v69
	v_mov_b32_e32 v35, v248
	v_cmpx_gt_i32_e32 34, v69
	v_mov_b32_e32 v34, v248
	v_cmpx_gt_i32_e32 33, v69
	v_mov_b32_e32 v33, v248
	v_cmpx_gt_i32_e32 32, v69
	v_mov_b32_e32 v32, v248
	v_cmpx_gt_i32_e32 27, v69
	v_mov_b32_e32 v63, v248
	v_cmpx_gt_i32_e32 26, v69
	v_mov_b32_e32 v62, v248
	v_cmpx_gt_i32_e32 25, v69
	v_mov_b32_e32 v61, v248
	v_cmpx_gt_i32_e32 24, v69
	v_mov_b32_e32 v60, v248
	v_cmpx_gt_i32_e32 19, v69
	v_mov_b32_e32 v59, v248
	v_cmpx_gt_i32_e32 18, v69
	v_mov_b32_e32 v58, v248
	v_cmpx_gt_i32_e32 17, v69
	v_mov_b32_e32 v57, v248
	v_cmpx_gt_i32_e32 16, v69
	v_mov_b32_e32 v56, v248
	v_cmpx_gt_i32_e32 11, v69
	v_mov_b32_e32 v55, v248
	v_cmpx_gt_i32_e32 10, v69
	v_mov_b32_e32 v54, v248
	v_cmpx_gt_i32_e32 9, v69
	v_mov_b32_e32 v53, v248
	v_cmpx_gt_i32_e32 8, v69
	v_mov_b32_e32 v52, v248
	v_cmpx_gt_i32_e32 3, v69
	v_mov_b32_e32 v51, v248
	v_cmpx_gt_i32_e32 2, v69
	v_mov_b32_e32 v50, v248
	v_cmpx_gt_i32_e32 1, v69
	v_mov_b32_e32 v49, v248
	v_cmpx_gt_i32_e32 0, v69
	v_mov_b32_e32 v48, v248
	s_mov_b64 exec, s[100:101]
	s_nop 4

; __device__ __forceinline__ void cmask(f32x16& p0, f32x16& p1, int jb, int qrel, int hi) {
;     const float NEG = -INFINITY; int kb = 64 * jb + 4 * hi;
; #pragma unroll
;     for (int r = 0; r < 16; ++r) { int kv = kb + (r & 3) + 8 * (r >> 2); if (kv > qrel) p0[r] = NEG; if (kv + 32 > qrel) p1[r] = NEG; }
; }
.LBB0_630:
	s_add_i32 s11, s68, 0x2000
	s_cmpk_lg_i32 s68, 0x4000
	s_cselect_b32 s11, s11, 0
	v_add_u32_e32 v160, s69, v229
	ds_read_b64_tr_b16 v[156:157], v160 offset:24576
	ds_read_b64_tr_b16 v[158:159], v160 offset:25088
	v_mfma_f32_32x32x16_f16 v[80:95], v[188:191], v[128:131], v[80:95]
	v_add_f32_e32 v132, v48, v49
	v_add_f32_e32 v132, v50, v132
	v_add_f32_e32 v132, v51, v132
	v_add_f32_e32 v132, v52, v132
	v_add_f32_e32 v132, v53, v132
	v_cvt_pk_f16_f32 v144, v48, v49
	v_cvt_pk_f16_f32 v145, v50, v51
	ds_read_b64_tr_b16 v[152:153], v160 offset:28672
	ds_read_b64_tr_b16 v[154:155], v160 offset:29184
	v_mfma_f32_32x32x16_f16 v[64:79], v[148:151], v[128:131], v[64:79]
	v_add_f32_e32 v48, v54, v132
	v_add_f32_e32 v48, v55, v48
	v_add_f32_e32 v48, v56, v48
	v_add_f32_e32 v48, v57, v48
	v_cvt_pk_f16_f32 v146, v52, v53
	v_cvt_pk_f16_f32 v147, v54, v55
	ds_read_b64_tr_b16 v[148:149], v160 offset:25600
	ds_read_b64_tr_b16 v[150:151], v160 offset:26112
	v_mfma_f32_32x32x16_f16 v[80:95], v[184:187], v[124:127], v[80:95]
	v_add_f32_e32 v48, v58, v48
	v_add_f32_e32 v48, v59, v48
	v_add_f32_e32 v48, v60, v48
	v_add_f32_e32 v48, v61, v48
	v_cvt_pk_f16_f32 v140, v56, v57
	v_cvt_pk_f16_f32 v141, v58, v59
	ds_read_b64_tr_b16 v[52:53], v160 offset:29696
	ds_read_b64_tr_b16 v[54:55], v160 offset:30208
	v_mfma_f32_32x32x16_f16 v[64:79], v[172:175], v[124:127], v[64:79]
	v_add_f32_e32 v48, v62, v48
	v_add_f32_e32 v48, v63, v48
	v_add_f32_e32 v48, v32, v48
	v_add_f32_e32 v56, v33, v48
	v_cvt_pk_f16_f32 v142, v60, v61
	v_cvt_pk_f16_f32 v143, v62, v63
	ds_read_b64_tr_b16 v[48:49], v160 offset:26624
	ds_read_b64_tr_b16 v[50:51], v160 offset:27136
	s_waitcnt lgkmcnt(13)
	v_mfma_f32_32x32x16_f16 v[80:95], v[176:179], v[120:123], v[80:95]
	v_add_f32_e32 v56, v34, v56
	v_add_f32_e32 v56, v35, v56
	v_add_f32_e32 v56, v36, v56
	v_add_f32_e32 v56, v37, v56
	v_cvt_pk_f16_f32 v136, v32, v33
	v_cvt_pk_f16_f32 v137, v34, v35
	ds_read_b64_tr_b16 v[184:185], v160 offset:30720
	ds_read_b64_tr_b16 v[186:187], v160 offset:31232
	s_waitcnt lgkmcnt(14)
	v_mfma_f32_32x32x16_f16 v[64:79], v[164:167], v[120:123], v[64:79]
	v_add_f32_e32 v32, v38, v56
	v_add_f32_e32 v32, v39, v32
	v_add_f32_e32 v32, v40, v32
	v_add_f32_e32 v56, v41, v32
	v_cvt_pk_f16_f32 v138, v36, v37
	v_cvt_pk_f16_f32 v139, v38, v39
	ds_read_b64_tr_b16 v[32:33], v160 offset:27648
	ds_read_b64_tr_b16 v[34:35], v160 offset:28160
	s_waitcnt lgkmcnt(14)
	v_mfma_f32_32x32x16_f16 v[80:95], v[180:183], v[116:119], v[80:95]
	v_add_f32_e32 v36, v42, v56
	v_add_f32_e32 v36, v43, v36
	v_add_f32_e32 v36, v44, v36
	v_add_f32_e32 v36, v45, v36
	v_cvt_pk_f16_f32 v132, v40, v41
	v_cvt_pk_f16_f32 v133, v42, v43
	ds_read_b64_tr_b16 v[180:181], v160 offset:31744
	ds_read_b64_tr_b16 v[182:183], v160 offset:32256
	v_mfma_f32_32x32x16_f16 v[64:79], v[168:171], v[116:119], v[64:79]
	v_add_f32_e32 v36, v46, v36
	v_add_f32_e32 v36, v47, v36
	v_add_f32_e32 v36, 0, v36
	v_cvt_pk_f16_f32 v134, v44, v45
	v_cvt_pk_f16_f32 v135, v46, v47
	s_add_i32 s50, s68, s90
	s_add_i32 s18, s18, 2
	s_cmp_lt_u32 s45, 2
	s_mov_b32 s51, m0
	s_mov_b32 m0, s50
	s_nop 0
	global_load_lds_dwordx4 v[194:195], off
	s_mov_b32 m0, s51
	s_cselect_b32 s18, s18, s37
	v_mad_i64_i32 v[38:39], s[50:51], s18, v249, v[216:217]
	s_add_i32 s37, s11, s10
	s_mov_b32 s50, m0
	s_mov_b32 m0, s37
	s_nop 0
	global_load_lds_dwordx4 v[38:39], off
	s_mov_b32 m0, s50
	s_andn2_b64 vcc, exec, s[40:41]
	s_cbranch_vccnz .LBB0_632
	s_mov_b64 s[100:101], exec
	v_sub_u32_e32 v38, v215, v196
	v_add_u32_e32 v38, 0xffffffe0, v38
	v_cmpx_gt_i32_e32 59, v38
	v_mov_b32_e32 v79, v248
	v_cmpx_gt_i32_e32 58, v38
	v_mov_b32_e32 v78, v248
	v_cmpx_gt_i32_e32 57, v38
	v_mov_b32_e32 v77, v248
	v_cmpx_gt_i32_e32 56, v38
	v_mov_b32_e32 v76, v248
	v_cmpx_gt_i32_e32 51, v38
	v_mov_b32_e32 v75, v248
	v_cmpx_gt_i32_e32 50, v38
	v_mov_b32_e32 v74, v248
	v_cmpx_gt_i32_e32 49, v38
	v_mov_b32_e32 v73, v248
	v_cmpx_gt_i32_e32 48, v38
	v_mov_b32_e32 v72, v248
	v_cmpx_gt_i32_e32 43, v38
	v_mov_b32_e32 v71, v248
	v_cmpx_gt_i32_e32 42, v38
	v_mov_b32_e32 v70, v248
	v_cmpx_gt_i32_e32 41, v38
	v_mov_b32_e32 v69, v248
	v_cmpx_gt_i32_e32 40, v38
	v_mov_b32_e32 v68, v248
	v_cmpx_gt_i32_e32 35, v38
	v_mov_b32_e32 v67, v248
	v_cmpx_gt_i32_e32 34, v38
	v_mov_b32_e32 v66, v248
	v_cmpx_gt_i32_e32 33, v38
	v_mov_b32_e32 v65, v248
	v_cmpx_gt_i32_e32 32, v38
	v_mov_b32_e32 v64, v248
	v_cmpx_gt_i32_e32 27, v38
	v_mov_b32_e32 v95, v248
	v_cmpx_gt_i32_e32 26, v38
	v_mov_b32_e32 v94, v248
	v_cmpx_gt_i32_e32 25, v38
	v_mov_b32_e32 v93, v248
	v_cmpx_gt_i32_e32 24, v38
	v_mov_b32_e32 v92, v248
	v_cmpx_gt_i32_e32 19, v38
	v_mov_b32_e32 v91, v248
	v_cmpx_gt_i32_e32 18, v38
	v_mov_b32_e32 v90, v248
	v_cmpx_gt_i32_e32 17, v38
	v_mov_b32_e32 v89, v248
	v_cmpx_gt_i32_e32 16, v38
	v_mov_b32_e32 v88, v248
	v_cmpx_gt_i32_e32 11, v38
	v_mov_b32_e32 v87, v248
	v_cmpx_gt_i32_e32 10, v38
	v_mov_b32_e32 v86, v248
	v_cmpx_gt_i32_e32 9, v38
	v_mov_b32_e32 v85, v248
	v_cmpx_gt_i32_e32 8, v38
	v_mov_b32_e32 v84, v248
	v_cmpx_gt_i32_e32 3, v38
	v_mov_b32_e32 v83, v248
	v_cmpx_gt_i32_e32 2, v38
	v_mov_b32_e32 v82, v248
	v_cmpx_gt_i32_e32 1, v38
	v_mov_b32_e32 v81, v248
	v_cmpx_gt_i32_e32 0, v38
	v_mov_b32_e32 v80, v248
	s_mov_b64 exec, s[100:101]
	s_nop 4

; __device__ __forceinline__ void cmask(f32x16& p0, f32x16& p1, int jb, int qrel, int hi) {
;     const float NEG = -INFINITY; int kb = 64 * jb + 4 * hi;
; #pragma unroll
;     for (int r = 0; r < 16; ++r) { int kv = kb + (r & 3) + 8 * (r >> 2); if (kv > qrel) p0[r] = NEG; if (kv + 32 > qrel) p1[r] = NEG; }
; }
.LBB0_648:
	s_add_i32 s28, s26, s37
	s_add_i32 s45, s28, 1
	s_cmp_lt_u32 s37, 3
	s_cselect_b64 s[40:41], -1, 0
	s_and_b64 s[66:67], s[40:41], exec
	s_cselect_b32 s45, s45, s19
	v_mad_i64_i32 v[70:71], s[66:67], s45, v249, v[216:217]
	s_add_i32 s66, s18, s10
	s_mov_b32 s67, m0
	s_mov_b32 m0, s66
	s_nop 0
	global_load_lds_dwordx4 v[70:71], off
	s_mov_b32 m0, s67
	s_cmp_gt_u32 s37, 3
	s_cbranch_scc1 .LBB0_650
	s_mov_b64 s[100:101], exec
	v_sub_u32_e32 v70, v215, v234
	v_add_u32_e32 v70, 0x7b, v70
	v_cmpx_gt_i32_e32 59, v70
	v_mov_b32_e32 v47, v248
	v_cmpx_gt_i32_e32 58, v70
	v_mov_b32_e32 v46, v248
	v_cmpx_gt_i32_e32 57, v70
	v_mov_b32_e32 v45, v248
	v_cmpx_gt_i32_e32 56, v70
	v_mov_b32_e32 v44, v248
	v_cmpx_gt_i32_e32 51, v70
	v_mov_b32_e32 v43, v248
	v_cmpx_gt_i32_e32 50, v70
	v_mov_b32_e32 v42, v248
	v_cmpx_gt_i32_e32 49, v70
	v_mov_b32_e32 v41, v248
	v_cmpx_gt_i32_e32 48, v70
	v_mov_b32_e32 v40, v248
	v_cmpx_gt_i32_e32 43, v70
	v_mov_b32_e32 v39, v248
	v_cmpx_gt_i32_e32 42, v70
	v_mov_b32_e32 v38, v248
	v_cmpx_gt_i32_e32 41, v70
	v_mov_b32_e32 v37, v248
	v_cmpx_gt_i32_e32 40, v70
	v_mov_b32_e32 v36, v248
	v_cmpx_gt_i32_e32 35, v70
	v_mov_b32_e32 v35, v248
	v_cmpx_gt_i32_e32 34, v70
	v_mov_b32_e32 v34, v248
	v_cmpx_gt_i32_e32 33, v70
	v_mov_b32_e32 v33, v248
	v_cmpx_gt_i32_e32 32, v70
	v_mov_b32_e32 v32, v248
	v_cmpx_gt_i32_e32 27, v70
	v_mov_b32_e32 v63, v248
	v_cmpx_gt_i32_e32 26, v70
	v_mov_b32_e32 v62, v248
	v_cmpx_gt_i32_e32 25, v70
	v_mov_b32_e32 v61, v248
	v_cmpx_gt_i32_e32 24, v70
	v_mov_b32_e32 v60, v248
	v_cmpx_gt_i32_e32 19, v70
	v_mov_b32_e32 v59, v248
	v_cmpx_gt_i32_e32 18, v70
	v_mov_b32_e32 v58, v248
	v_cmpx_gt_i32_e32 17, v70
	v_mov_b32_e32 v57, v248
	v_cmpx_gt_i32_e32 16, v70
	v_mov_b32_e32 v56, v248
	v_cmpx_gt_i32_e32 11, v70
	v_mov_b32_e32 v55, v248
	v_cmpx_gt_i32_e32 10, v70
	v_mov_b32_e32 v54, v248
	v_cmpx_gt_i32_e32 9, v70
	v_mov_b32_e32 v53, v248
	v_cmpx_gt_i32_e32 8, v70
	v_mov_b32_e32 v52, v248
	v_cmpx_gt_i32_e32 3, v70
	v_mov_b32_e32 v51, v248
	v_cmpx_gt_i32_e32 2, v70
	v_mov_b32_e32 v50, v248
	v_cmpx_gt_i32_e32 1, v70
	v_mov_b32_e32 v49, v248
	v_cmpx_gt_i32_e32 0, v70
	v_mov_b32_e32 v48, v248
	s_mov_b64 exec, s[100:101]
	s_nop 4

; __device__ __forceinline__ void cmask(f32x16& p0, f32x16& p1, int jb, int qrel, int hi) {
;     const float NEG = -INFINITY; int kb = 64 * jb + 4 * hi;
; #pragma unroll
;     for (int r = 0; r < 16; ++r) { int kv = kb + (r & 3) + 8 * (r >> 2); if (kv > qrel) p0[r] = NEG; if (kv + 32 > qrel) p1[r] = NEG; }
; }
.LBB0_659:
	s_andn2_b64 vcc, exec, s[40:41]
	s_cbranch_vccnz .LBB0_661
	s_mov_b64 s[100:101], exec
	v_sub_u32_e32 v237, v215, v234
	v_add_u32_e32 v237, 59, v237
	v_cmpx_gt_i32_e32 59, v237
	v_mov_b32_e32 v79, v248
	v_cmpx_gt_i32_e32 58, v237
	v_mov_b32_e32 v78, v248
	v_cmpx_gt_i32_e32 57, v237
	v_mov_b32_e32 v77, v248
	v_cmpx_gt_i32_e32 56, v237
	v_mov_b32_e32 v76, v248
	v_cmpx_gt_i32_e32 51, v237
	v_mov_b32_e32 v75, v248
	v_cmpx_gt_i32_e32 50, v237
	v_mov_b32_e32 v74, v248
	v_cmpx_gt_i32_e32 49, v237
	v_mov_b32_e32 v73, v248
	v_cmpx_gt_i32_e32 48, v237
	v_mov_b32_e32 v72, v248
	v_cmpx_gt_i32_e32 43, v237
	v_mov_b32_e32 v71, v248
	v_cmpx_gt_i32_e32 42, v237
	v_mov_b32_e32 v70, v248
	v_cmpx_gt_i32_e32 41, v237
	v_mov_b32_e32 v69, v248
	v_cmpx_gt_i32_e32 40, v237
	v_mov_b32_e32 v68, v248
	v_cmpx_gt_i32_e32 35, v237
	v_mov_b32_e32 v67, v248
	v_cmpx_gt_i32_e32 34, v237
	v_mov_b32_e32 v66, v248
	v_cmpx_gt_i32_e32 33, v237
	v_mov_b32_e32 v65, v248
	v_cmpx_gt_i32_e32 32, v237
	v_mov_b32_e32 v64, v248
	v_cmpx_gt_i32_e32 27, v237
	v_mov_b32_e32 v95, v248
	v_cmpx_gt_i32_e32 26, v237
	v_mov_b32_e32 v94, v248
	v_cmpx_gt_i32_e32 25, v237
	v_mov_b32_e32 v93, v248
	v_cmpx_gt_i32_e32 24, v237
	v_mov_b32_e32 v92, v248
	v_cmpx_gt_i32_e32 19, v237
	v_mov_b32_e32 v91, v248
	v_cmpx_gt_i32_e32 18, v237
	v_mov_b32_e32 v90, v248
	v_cmpx_gt_i32_e32 17, v237
	v_mov_b32_e32 v89, v248
	v_cmpx_gt_i32_e32 16, v237
	v_mov_b32_e32 v88, v248
	v_cmpx_gt_i32_e32 11, v237
	v_mov_b32_e32 v87, v248
	v_cmpx_gt_i32_e32 10, v237
	v_mov_b32_e32 v86, v248
	v_cmpx_gt_i32_e32 9, v237
	v_mov_b32_e32 v85, v248
	v_cmpx_gt_i32_e32 8, v237
	v_mov_b32_e32 v84, v248
	v_cmpx_gt_i32_e32 3, v237
	v_mov_b32_e32 v83, v248
	v_cmpx_gt_i32_e32 2, v237
	v_mov_b32_e32 v82, v248
	v_cmpx_gt_i32_e32 1, v237
	v_mov_b32_e32 v81, v248
	v_cmpx_gt_i32_e32 0, v237
	v_mov_b32_e32 v80, v248
	s_mov_b64 exec, s[100:101]
	s_nop 4

; __device__ __forceinline__ void cmask(f32x16& p0, f32x16& p1, int jb, int qrel, int hi) {
;     const float NEG = -INFINITY; int kb = 64 * jb + 4 * hi;
; #pragma unroll
;     for (int r = 0; r < 16; ++r) { int kv = kb + (r & 3) + 8 * (r >> 2); if (kv > qrel) p0[r] = NEG; if (kv + 32 > qrel) p1[r] = NEG; }
; }
.LBB0_711:
	v_add_u32_e32 v184, s18, v229
	ds_read_b64_tr_b16 v[180:181], v184 offset:24576
	ds_read_b64_tr_b16 v[182:183], v184 offset:25088
	s_waitcnt lgkmcnt(9)
	v_mfma_f32_32x32x16_f16 v[48:63], v[176:179], v[128:131], v[48:63]
	v_add_f32_e32 v132, v80, v81
	v_add_f32_e32 v132, v82, v132
	v_add_f32_e32 v132, v83, v132
	v_add_f32_e32 v132, v84, v132
	v_add_f32_e32 v132, v85, v132
	v_cvt_pk_f16_f32 v144, v80, v81
	v_cvt_pk_f16_f32 v145, v82, v83
	ds_read_b64_tr_b16 v[80:81], v184 offset:28672
	ds_read_b64_tr_b16 v[82:83], v184 offset:29184
	s_waitcnt lgkmcnt(10)
	v_mfma_f32_32x32x16_f16 v[32:47], v[172:175], v[128:131], v[32:47]
	v_add_f32_e32 v128, v86, v132
	v_add_f32_e32 v128, v87, v128
	v_add_f32_e32 v128, v88, v128
	v_add_f32_e32 v128, v89, v128
	v_cvt_pk_f16_f32 v146, v84, v85
	v_cvt_pk_f16_f32 v147, v86, v87
	ds_read_b64_tr_b16 v[84:85], v184 offset:25600
	ds_read_b64_tr_b16 v[86:87], v184 offset:26112
	s_waitcnt lgkmcnt(11)
	v_mfma_f32_32x32x16_f16 v[48:63], v[168:171], v[124:127], v[48:63]
	v_add_f32_e32 v128, v90, v128
	v_add_f32_e32 v128, v91, v128
	v_add_f32_e32 v128, v92, v128
	v_add_f32_e32 v128, v93, v128
	v_cvt_pk_f16_f32 v140, v88, v89
	v_cvt_pk_f16_f32 v141, v90, v91
	ds_read_b64_tr_b16 v[88:89], v184 offset:29696
	ds_read_b64_tr_b16 v[90:91], v184 offset:30208
	s_waitcnt lgkmcnt(12)
	v_mfma_f32_32x32x16_f16 v[32:47], v[164:167], v[124:127], v[32:47]
	v_add_f32_e32 v124, v94, v128
	v_add_f32_e32 v124, v95, v124
	v_add_f32_e32 v124, v64, v124
	v_add_f32_e32 v124, v65, v124
	v_cvt_pk_f16_f32 v142, v92, v93
	v_cvt_pk_f16_f32 v143, v94, v95
	ds_read_b64_tr_b16 v[92:93], v184 offset:26624
	ds_read_b64_tr_b16 v[94:95], v184 offset:27136
	s_waitcnt lgkmcnt(13)
	v_mfma_f32_32x32x16_f16 v[48:63], v[160:163], v[120:123], v[48:63]
	v_add_f32_e32 v124, v66, v124
	v_add_f32_e32 v124, v67, v124
	v_add_f32_e32 v124, v68, v124
	v_add_f32_e32 v124, v69, v124
	v_cvt_pk_f16_f32 v136, v64, v65
	v_cvt_pk_f16_f32 v137, v66, v67
	ds_read_b64_tr_b16 v[64:65], v184 offset:30720
	ds_read_b64_tr_b16 v[66:67], v184 offset:31232
	s_waitcnt lgkmcnt(14)
	v_mfma_f32_32x32x16_f16 v[32:47], v[152:155], v[120:123], v[32:47]
	v_add_f32_e32 v120, v70, v124
	v_add_f32_e32 v120, v71, v120
	v_add_f32_e32 v120, v72, v120
	v_add_f32_e32 v120, v73, v120
	v_cvt_pk_f16_f32 v138, v68, v69
	v_cvt_pk_f16_f32 v139, v70, v71
	ds_read_b64_tr_b16 v[68:69], v184 offset:27648
	ds_read_b64_tr_b16 v[70:71], v184 offset:28160
	s_waitcnt lgkmcnt(14)
	v_mfma_f32_32x32x16_f16 v[48:63], v[156:159], v[116:119], v[48:63]
	v_add_f32_e32 v120, v74, v120
	v_add_f32_e32 v120, v75, v120
	v_add_f32_e32 v120, v76, v120
	v_add_f32_e32 v120, v77, v120
	v_cvt_pk_f16_f32 v132, v72, v73
	v_cvt_pk_f16_f32 v133, v74, v75
	ds_read_b64_tr_b16 v[72:73], v184 offset:31744
	ds_read_b64_tr_b16 v[74:75], v184 offset:32256
	v_mfma_f32_32x32x16_f16 v[32:47], v[148:151], v[116:119], v[32:47]
	v_add_f32_e32 v116, v78, v120
	v_add_f32_e32 v116, v79, v116
	v_add_f32_e32 v116, 0, v116
	v_cvt_pk_f16_f32 v134, v76, v77
	v_cvt_pk_f16_f32 v135, v78, v79
	s_andn2_b64 vcc, exec, s[0:1]
	s_cbranch_vccnz .LBB0_713
	s_mov_b64 s[100:101], exec
	v_sub_u32_e32 v77, v215, v231
	v_add_u32_e32 v77, 0xffffff40, v77
	v_cmpx_gt_i32_e32 59, v77
	v_mov_b32_e32 v47, v248
	v_cmpx_gt_i32_e32 58, v77
	v_mov_b32_e32 v46, v248
	v_cmpx_gt_i32_e32 57, v77
	v_mov_b32_e32 v45, v248
	v_cmpx_gt_i32_e32 56, v77
	v_mov_b32_e32 v44, v248
	v_cmpx_gt_i32_e32 51, v77
	v_mov_b32_e32 v43, v248
	v_cmpx_gt_i32_e32 50, v77
	v_mov_b32_e32 v42, v248
	v_cmpx_gt_i32_e32 49, v77
	v_mov_b32_e32 v41, v248
	v_cmpx_gt_i32_e32 48, v77
	v_mov_b32_e32 v40, v248
	v_cmpx_gt_i32_e32 43, v77
	v_mov_b32_e32 v39, v248
	v_cmpx_gt_i32_e32 42, v77
	v_mov_b32_e32 v38, v248
	v_cmpx_gt_i32_e32 41, v77
	v_mov_b32_e32 v37, v248
	v_cmpx_gt_i32_e32 40, v77
	v_mov_b32_e32 v36, v248
	v_cmpx_gt_i32_e32 35, v77
	v_mov_b32_e32 v35, v248
	v_cmpx_gt_i32_e32 34, v77
	v_mov_b32_e32 v34, v248
	v_cmpx_gt_i32_e32 33, v77
	v_mov_b32_e32 v33, v248
	v_cmpx_gt_i32_e32 32, v77
	v_mov_b32_e32 v32, v248
	v_cmpx_gt_i32_e32 27, v77
	v_mov_b32_e32 v63, v248
	v_cmpx_gt_i32_e32 26, v77
	v_mov_b32_e32 v62, v248
	v_cmpx_gt_i32_e32 25, v77
	v_mov_b32_e32 v61, v248
	v_cmpx_gt_i32_e32 24, v77
	v_mov_b32_e32 v60, v248
	v_cmpx_gt_i32_e32 19, v77
	v_mov_b32_e32 v59, v248
	v_cmpx_gt_i32_e32 18, v77
	v_mov_b32_e32 v58, v248
	v_cmpx_gt_i32_e32 17, v77
	v_mov_b32_e32 v57, v248
	v_cmpx_gt_i32_e32 16, v77
	v_mov_b32_e32 v56, v248
	v_cmpx_gt_i32_e32 11, v77
	v_mov_b32_e32 v55, v248
	v_cmpx_gt_i32_e32 10, v77
	v_mov_b32_e32 v54, v248
	v_cmpx_gt_i32_e32 9, v77
	v_mov_b32_e32 v53, v248
	v_cmpx_gt_i32_e32 8, v77
	v_mov_b32_e32 v52, v248
	v_cmpx_gt_i32_e32 3, v77
	v_mov_b32_e32 v51, v248
	v_cmpx_gt_i32_e32 2, v77
	v_mov_b32_e32 v50, v248
	v_cmpx_gt_i32_e32 1, v77
	v_mov_b32_e32 v49, v248
	v_cmpx_gt_i32_e32 0, v77
	v_mov_b32_e32 v48, v248
	s_mov_b64 exec, s[100:101]
	s_nop 4
